# s16p + layer-1 norm1 gate-column dot products: the 128 LDS weight reads issued eight ahead into a rotating pool of fresh VGPR quads (was a two-deep ping-pong waited a few VALU later); arithmetic uncha
# speedup vs baseline: 1.0047x; 1.0011x over previous
; DI unsigned pk2(float lo, float hi) { const f32x2 v = {lo, hi}; return __builtin_bit_cast(unsigned, __builtin_convertvector(v, bf16x2_t)); }
; template <int MODE, bool SB  > DI void norm_phase(const Params& P, const Frame& F, int L, const void* src_, const float* gain, bool combine) {
;     ...
;     for (int row = r_lo + F.wave; row < r_hi; row += NWAVES) {
;         f32x4 v[8];
; #pragma unroll
;         for (int j = 0; j < 8; ++j) { if constexpr (SB) v[j] = (f32x4){bflo(vb[j].x), bfhi(vb[j].x), bflo(vb[j].y), bfhi(vb[j].y)}; else v[j] = vn[j]; }
;         { const int rnx = (row + NWAVES < r_hi) ? row + NWAVES : row;
; #pragma unroll
;           for (int j = 0; j < 8; ++j) { if constexpr (SB) vb[j] = *(const u32x2*)(srcb + (size_t)rnx * D + 4 * F.lane + 256 * j); else vn[j] = *(const f32x4*)(src + (size_t)rnx * D + 4 * F.lane + 256 * j); } }
;         if (MODE == 3 && combine) {
;             const int* SLOT = (const int*)(ws + WS_SLOT); const float* TOPW = (const float*)(ws + WS_TOPW); const bf16* Y = (const bf16*)(ws + WS_T + T_YPERM);
;             const int s1 = SLOT[row * 2], s2 = SLOT[row * 2 + 1]; const float w1 = TOPW[row * 2], w2 = TOPW[row * 2 + 1];
;             u32x2 ya[8], yb[8];
; #pragma unroll
;             for (int j = 0; j < 8; ++j) { ya[j] = *(const u32x2*)(Y + (size_t)s1 * D + 4 * F.lane + 256 * j); yb[j] = *(const u32x2*)(Y + (size_t)s2 * D + 4 * F.lane + 256 * j); }
; #pragma unroll
;             for (int j = 0; j < 8; ++j) { const f32x4 y1 = (f32x4){bflo(ya[j].x), bfhi(ya[j].x), bflo(ya[j].y), bfhi(ya[j].y)}, y2 = (f32x4){bflo(yb[j].x), bfhi(yb[j].x), bflo(yb[j].y), bfhi(yb[j].y)};
;                 v[j] = v[j] + w1 * y1 + w2 * y2;
;                 const u32x2 hb = {pk2(v[j][0], v[j][1]), pk2(v[j][2], v[j][3])}; *(u32x2*)(const_cast<bf16*>(srcb) + (size_t)row * D + 4 * F.lane + 256 * j) = hb;
;                 v[j] = (f32x4){bflo(hb.x), bfhi(hb.x), bflo(hb.y), bfhi(hb.y)}; }
;         }
;         float ss = 0.f;
; #pragma unroll
;         for (int j = 0; j < 8; ++j) ss += (v[j][0] * v[j][0] + v[j][1] * v[j][1]) + (v[j][2] * v[j][2] + v[j][3] * v[j][3]);
;         const float rstd = 1.0f / sqrtf(wave_sum(ss) * (1.0f / D) + EPS);
; #pragma unroll
;         for (int j = 0; j < 8; ++j) v[j] = v[j] * rstd * g[j];
.LBB0_1648:
	s_waitcnt vmcnt(0)
	v_and_b32_e32 v75, 0xffff0000, v50
	v_and_b32_e32 v77, 0xffff0000, v51
	v_lshlrev_b32_e32 v65, 16, v48
	v_and_b32_e32 v69, 0xffff0000, v48
	v_lshlrev_b32_e32 v74, 16, v50
	v_lshlrev_b32_e32 v76, 16, v51
	v_mul_f32_e32 v48, v77, v77
	v_lshlrev_b32_e32 v78, 16, v52
	v_and_b32_e32 v81, 0xffff0000, v53
	v_and_b32_e32 v80, 0xffff0000, v52
	v_mul_f32_e32 v52, v75, v75
	v_lshlrev_b32_e32 v72, 16, v49
	v_and_b32_e32 v73, 0xffff0000, v49
	v_pk_fma_f32 v[48:49], v[76:77], v[76:77], v[48:49] op_sel_hi:[1,1,0]
	v_lshlrev_b32_e32 v79, 16, v53
	v_pk_mul_f32 v[50:51], v[80:81], v[80:81]
	v_pk_fma_f32 v[52:53], v[74:75], v[74:75], v[52:53] op_sel_hi:[1,1,0]
	v_pk_fma_f32 v[50:51], v[78:79], v[78:79], v[50:51]
	v_lshlrev_b32_e32 v82, 16, v54
	v_and_b32_e32 v83, 0xffff0000, v54
	v_lshlrev_b32_e32 v84, 16, v55
	v_and_b32_e32 v85, 0xffff0000, v55
	v_mov_b32_e32 v64, v52
	v_mov_b32_e32 v54, v48
	v_mov_b32_e32 v55, v65
	v_mul_f32_e32 v47, v69, v69
	v_pk_add_f32 v[48:49], v[52:53], v[48:49]
	v_pk_mul_f32 v[52:53], v[64:65], v[54:55]
	v_pk_add_f32 v[50:51], v[50:51], v[50:51] op_sel:[0,1] op_sel_hi:[1,0]
	v_mov_b32_e32 v49, v53
	v_mov_b32_e32 v51, v47
	v_pk_add_f32 v[48:49], v[48:49], v[50:51]
	v_mul_f32_e32 v50, v83, v83
	v_mul_f32_e32 v52, v85, v85
	v_lshlrev_b32_e32 v97, 16, v56
	v_and_b32_e32 v71, 0xffff0000, v56
	v_lshlrev_b32_e32 v66, 16, v57
	v_and_b32_e32 v67, 0xffff0000, v57
	v_mul_f32_e32 v56, v72, v72
	v_mul_f32_e32 v57, v73, v73
	v_pk_fma_f32 v[50:51], v[82:83], v[82:83], v[50:51] op_sel_hi:[1,1,0]
	v_pk_fma_f32 v[52:53], v[84:85], v[84:85], v[52:53] op_sel_hi:[1,1,0]
	v_mov_b32_e32 v51, v56
	v_mov_b32_e32 v53, v57
	v_pk_add_f32 v[50:51], v[50:51], v[52:53]
	v_and_b32_e32 v173, 0xffff0000, v59
	v_and_b32_e32 v172, 0xffff0000, v58
	v_pk_add_f32 v[48:49], v[48:49], v[50:51]
	v_lshlrev_b32_e32 v171, 16, v59
	v_lshlrev_b32_e32 v170, 16, v58
	v_pk_mul_f32 v[50:51], v[172:173], v[172:173]
	v_and_b32_e32 v177, 0xffff0000, v61
	v_pk_fma_f32 v[50:51], v[170:171], v[170:171], v[50:51]
	v_and_b32_e32 v176, 0xffff0000, v60
	v_pk_add_f32 v[50:51], v[50:51], v[50:51] op_sel:[0,1] op_sel_hi:[1,0]
	v_pk_add_f32 v[48:49], v[48:49], v[48:49] op_sel:[0,1] op_sel_hi:[1,0]
	v_lshlrev_b32_e32 v175, 16, v61
	v_lshlrev_b32_e32 v174, 16, v60
	v_pk_mul_f32 v[52:53], v[176:177], v[176:177]
	v_mov_b32_e32 v96, v48
	v_mov_b32_e32 v54, v50
	v_mov_b32_e32 v55, v97
	v_pk_fma_f32 v[52:53], v[174:175], v[174:175], v[52:53]
	v_pk_add_f32 v[48:49], v[48:49], v[50:51]
	v_pk_mul_f32 v[50:51], v[96:97], v[54:55]
	v_mul_f32_e32 v47, v71, v71
	v_mov_b32_e32 v49, v51
	v_pk_add_f32 v[50:51], v[52:53], v[52:53] op_sel:[0,1] op_sel_hi:[1,0]
	v_and_b32_e32 v179, 0xffff0000, v62
	v_and_b32_e32 v181, 0xffff0000, v63
	v_mov_b32_e32 v51, v47
	v_lshlrev_b32_e32 v178, 16, v62
	v_lshlrev_b32_e32 v180, 16, v63
	v_pk_add_f32 v[48:49], v[48:49], v[50:51]
	v_mul_f32_e32 v50, v179, v179
	v_mul_f32_e32 v52, v181, v181
	v_mul_f32_e32 v56, v66, v66
	v_mul_f32_e32 v57, v67, v67
	v_pk_fma_f32 v[50:51], v[178:179], v[178:179], v[50:51] op_sel_hi:[1,1,0]
	v_pk_fma_f32 v[52:53], v[180:181], v[180:181], v[52:53] op_sel_hi:[1,1,0]
	v_mov_b32_e32 v51, v56
	v_mov_b32_e32 v53, v57
	v_pk_add_f32 v[50:51], v[50:51], v[52:53]
	s_mov_b32 s20, s0
	v_pk_add_f32 v[48:49], v[48:49], v[50:51]
	s_add_i32 s0, s0, 8
	v_add_f32_e32 v47, v48, v49
	s_cmp_ge_i32 s0, s3
	s_cselect_b64 s[22:23], -1, 0
	v_add_f32_dpp v47, v47, v47 quad_perm:[1,0,3,2] row_mask:0xf bank_mask:0xf bound_ctrl:1
	s_cmp_lt_i32 s0, s3
	s_cselect_b32 s20, s0, s20
	v_add_f32_dpp v47, v47, v47 quad_perm:[2,3,0,1] row_mask:0xf bank_mask:0xf bound_ctrl:1
	ds_swizzle_b32 v48, v47 offset:swizzle(SWAP,4)
	s_ashr_i32 s21, s20, 31
	s_lshl_b64 s[20:21], s[20:21], 12
	v_lshl_add_u64 v[56:57], v[32:33], 0, s[20:21]
	s_mov_b32 s20, 0xf800000
	s_waitcnt lgkmcnt(0)
	v_add_f32_e32 v47, v47, v48
	ds_swizzle_b32 v48, v47 offset:swizzle(SWAP,8)
	s_waitcnt lgkmcnt(0)
	v_add_f32_e32 v47, v47, v48
	ds_swizzle_b32 v48, v47 offset:swizzle(SWAP,16)
	s_waitcnt lgkmcnt(0)
	v_add_f32_e32 v47, v47, v48
	ds_bpermute_b32 v48, v98, v47
	s_waitcnt lgkmcnt(0)
	v_add_f32_e32 v47, v47, v48
	v_fmamk_f32 v47, v47, 0x3a000000, v164
	v_mul_f32_e32 v48, 0x4f800000, v47
	v_cmp_gt_f32_e32 vcc, s20, v47
	s_nop 1
	v_cndmask_b32_e32 v47, v47, v48, vcc
	v_sqrt_f32_e32 v58, v47
	global_load_dwordx2 v[50:51], v[56:57], off
	global_load_dwordx2 v[52:53], v[56:57], off offset:512
	global_load_dwordx2 v[54:55], v[56:57], off offset:1024
	global_load_dwordx2 v[48:49], v[56:57], off offset:1536
	v_add_u32_e32 v59, -1, v58
	v_fma_f32 v60, -v59, v58, v47
	v_cmp_ge_f32_e64 s[20:21], 0, v60
	v_add_u32_e32 v60, 1, v58
	s_nop 0
	v_cndmask_b32_e64 v59, v58, v59, s[20:21]
	v_fma_f32 v58, -v60, v58, v47
	v_cmp_lt_f32_e64 s[20:21], 0, v58
	s_nop 1
	v_cndmask_b32_e64 v58, v59, v60, s[20:21]
	v_mul_f32_e32 v59, 0x37800000, v58
	v_cndmask_b32_e32 v58, v58, v59, vcc
	v_cmp_class_f32_e32 vcc, v47, v165
	s_nop 1
	v_cndmask_b32_e32 v47, v58, v47, vcc
	v_div_scale_f32 v64, s[20:21], v47, v47, 1.0
	v_rcp_f32_e32 v68, v64
	s_mov_b32 s20, 0x3d600000
	global_load_dwordx2 v[58:59], v[56:57], off offset:2048
	global_load_dwordx2 v[60:61], v[56:57], off offset:2560
	global_load_dwordx2 v[62:63], v[56:57], off offset:3072
	s_nop 0
	global_load_dwordx2 v[56:57], v[56:57], off offset:3584
	v_fma_f32 v70, -v64, v68, 1.0
	v_fmac_f32_e32 v68, v70, v68
	v_div_scale_f32 v70, vcc, 1.0, v47, 1.0
	v_mul_f32_e32 v86, v70, v68
	v_fma_f32 v87, -v64, v86, v70
	v_fmac_f32_e32 v86, v87, v68
	v_fma_f32 v64, -v64, v86, v70
	v_div_fmas_f32 v64, v64, v68, v86
	v_div_fixup_f32 v96, v64, v47, 1.0
	v_pk_mul_f32 v[74:75], v[96:97], v[74:75] op_sel_hi:[0,1]
; #define LAS __attribute__((address_space(3)))
; DI unsigned pk2(float lo, float hi) { const f32x2 v = {lo, hi}; return __builtin_bit_cast(unsigned, __builtin_convertvector(v, bf16x2_t)); }
; template <int MODE, bool SB  > DI void norm_phase(const Params& P, const Frame& F, int L, const void* src_, const float* gain, bool combine) {
;     ...
;             unsigned long long* o8 = (unsigned long long*)(HN + (size_t)row * D) + F.lane;
; #pragma unroll
;             for (int j = 0; j < 8; ++j) o8[64 * j] = (unsigned long long)pk2(v[j][0], v[j][1]) | ((unsigned long long)pk2(v[j][2], v[j][3]) << 32);
;         }
;         if (MODE == 1) {
;             float s[16];
; #pragma unroll
;             for (int q = 0; q < 16; ++q) { float t = 0.f;
; #pragma unroll
;                 for (int j = 0; j < 8; ++j) { const f32x4 w = *(const LAS f32x4*)(F.lds + (size_t)(q * D + 256 * j + 4 * F.lane) * 4); t += (v[j][0] * w[0] + v[j][1] * w[1]) + (v[j][2] * w[2] + v[j][3] * w[3]); }
;                 s[q] = t; if ((q & 3) == 3) asm volatile("" ::: "memory"); }
	v_mov_b32_e32 v68, v65
	v_pk_mul_f32 v[76:77], v[96:97], v[76:77] op_sel_hi:[0,1]
	v_pk_mul_f32 v[92:93], v[8:9], v[74:75]
	v_mov_b32_e32 v75, v80
	v_mov_b32_e32 v80, v79
	v_pk_mul_f32 v[64:65], v[68:69], v[96:97] op_sel_hi:[1,0]
	v_pk_mul_f32 v[90:91], v[10:11], v[76:77]
	v_mov_b32_e32 v74, v78
	v_pk_mul_f32 v[76:77], v[96:97], v[80:81] op_sel_hi:[0,1]
	v_pk_mul_f32 v[86:87], v[12:13], v[64:65]
	v_mov_b32_e32 v64, v170
	v_mov_b32_e32 v65, v172
	v_pk_mul_f32 v[74:75], v[96:97], v[74:75] op_sel_hi:[0,1]
	v_pk_mul_f32 v[88:89], v[2:3], v[76:77]
	v_pk_mul_f32 v[76:77], v[96:97], v[84:85] op_sel_hi:[0,1]
	v_pk_mul_f32 v[68:69], v[72:73], v[96:97] op_sel_hi:[1,0]
	v_pk_mul_f32 v[64:65], v[96:97], v[64:65] op_sel_hi:[0,1]
	v_mov_b32_e32 v172, v171
	v_pk_mul_f32 v[94:95], v[0:1], v[74:75]
	v_pk_mul_f32 v[74:75], v[96:97], v[82:83] op_sel_hi:[0,1]
	v_pk_mul_f32 v[82:83], v[6:7], v[76:77]
	v_pk_mul_f32 v[78:79], v[14:15], v[68:69]
	v_pk_mul_f32 v[68:69], v[96:97], v[172:173] op_sel_hi:[0,1]
	v_pk_mul_f32 v[76:77], v[16:17], v[64:65]
	v_mov_b32_e32 v64, v174
	v_mov_b32_e32 v65, v176
	v_mov_b32_e32 v176, v175
	v_pk_mul_f32 v[84:85], v[4:5], v[74:75]
	v_pk_mul_f32 v[74:75], v[18:19], v[68:69]
	v_pk_mul_f32 v[64:65], v[96:97], v[64:65] op_sel_hi:[0,1]
	v_pk_mul_f32 v[68:69], v[96:97], v[176:177] op_sel_hi:[0,1]
	v_mov_b32_e32 v70, v97
	v_pk_mul_f32 v[72:73], v[22:23], v[68:69]
	v_pk_mul_f32 v[80:81], v[20:21], v[64:65]
	v_pk_mul_f32 v[68:69], v[96:97], v[178:179] op_sel_hi:[0,1]
	v_pk_mul_f32 v[64:65], v[96:97], v[180:181] op_sel_hi:[0,1]
	v_pk_mul_f32 v[70:71], v[70:71], v[96:97] op_sel_hi:[1,0]
	v_pk_mul_f32 v[66:67], v[66:67], v[96:97] op_sel_hi:[1,0]
	v_lshl_add_u64 v[96:97], s[54:55], 0, v[44:45]
	v_add_co_u32_e32 v96, vcc, s20, v96
	v_cvt_pk_bf16_f32 v170, v92, v93
	v_cvt_pk_bf16_f32 v171, v90, v91
	v_addc_co_u32_e32 v97, vcc, 0, v97, vcc
	global_store_dwordx2 v[96:97], v[170:171], off
	v_cvt_pk_bf16_f32 v170, v94, v95
	v_cvt_pk_bf16_f32 v171, v88, v89
	global_store_dwordx2 v[96:97], v[170:171], off offset:512
	v_cvt_pk_bf16_f32 v170, v84, v85
	v_cvt_pk_bf16_f32 v171, v82, v83
	global_store_dwordx2 v[96:97], v[170:171], off offset:1024
	v_cvt_pk_bf16_f32 v170, v86, v87
	v_cvt_pk_bf16_f32 v171, v78, v79
	global_store_dwordx2 v[96:97], v[170:171], off offset:1536
	v_cvt_pk_bf16_f32 v170, v76, v77
	v_cvt_pk_bf16_f32 v171, v74, v75
	v_pk_mul_f32 v[64:65], v[26:27], v[64:65]
	v_pk_mul_f32 v[68:69], v[24:25], v[68:69]
	global_store_dwordx2 v[96:97], v[170:171], off offset:2048
	v_cvt_pk_bf16_f32 v170, v80, v81
	v_cvt_pk_bf16_f32 v171, v72, v73
	global_store_dwordx2 v[96:97], v[170:171], off offset:2560
	v_cvt_pk_bf16_f32 v170, v68, v69
	v_cvt_pk_bf16_f32 v171, v64, v65
	global_store_dwordx2 v[96:97], v[170:171], off offset:3072
	ds_read_b128 v[196:199], v99
	ds_read_b128 v[200:203], v99 offset:1024
	ds_read_b128 v[204:207], v99 offset:2048
	ds_read_b128 v[208:211], v99 offset:3072
	ds_read_b128 v[212:215], v99 offset:4096
	ds_read_b128 v[216:219], v99 offset:5120
	ds_read_b128 v[220:223], v99 offset:6144
	ds_read_b128 v[224:227], v99 offset:7168
	v_pk_mul_f32 v[66:67], v[30:31], v[66:67]
	v_pk_mul_f32 v[70:71], v[28:29], v[70:71]
	v_cvt_pk_bf16_f32 v175, v66, v67
	v_cvt_pk_bf16_f32 v174, v70, v71
	global_store_dwordx2 v[96:97], v[174:175], off offset:3584
	s_waitcnt lgkmcnt(7)
	v_mul_f32_e32 v47, v197, v93
	v_mul_f32_e32 v96, v199, v91
	v_fmac_f32_e32 v47, v196, v92
	v_fmac_f32_e32 v96, v198, v90
	ds_read_b128 v[196:199], v99 offset:8192
	v_add_f32_e32 v47, v47, v96
	s_waitcnt lgkmcnt(7)
	v_mul_f32_e32 v96, v95, v201
	v_mul_f32_e32 v97, v89, v203
	v_fmac_f32_e32 v96, v94, v200
	v_fmac_f32_e32 v97, v88, v202
	ds_read_b128 v[200:203], v99 offset:9216
	v_add_f32_e32 v47, 0, v47
	v_add_f32_e32 v96, v96, v97
	v_add_f32_e32 v47, v96, v47
	s_waitcnt lgkmcnt(7)
	v_mul_f32_e32 v96, v85, v205
	v_mul_f32_e32 v97, v83, v207
	v_fmac_f32_e32 v96, v84, v204
	v_fmac_f32_e32 v97, v82, v206
	ds_read_b128 v[204:207], v99 offset:10240
	v_add_f32_e32 v96, v96, v97
	v_add_f32_e32 v47, v96, v47
	s_waitcnt lgkmcnt(7)
	v_mul_f32_e32 v96, v87, v209
	v_mul_f32_e32 v97, v79, v211
	v_fmac_f32_e32 v96, v86, v208
	v_fmac_f32_e32 v97, v78, v210
	ds_read_b128 v[208:211], v99 offset:11264
	v_add_f32_e32 v96, v96, v97
	v_add_f32_e32 v47, v96, v47
	s_waitcnt lgkmcnt(7)
	v_mul_f32_e32 v96, v77, v213
	v_mul_f32_e32 v97, v75, v215
	v_fmac_f32_e32 v96, v76, v212
	v_fmac_f32_e32 v97, v74, v214
	ds_read_b128 v[212:215], v99 offset:12288
	v_add_f32_e32 v96, v96, v97
	v_add_f32_e32 v47, v96, v47
	s_waitcnt lgkmcnt(7)
	v_mul_f32_e32 v96, v81, v217
	v_mul_f32_e32 v97, v73, v219
	v_fmac_f32_e32 v96, v80, v216
	v_fmac_f32_e32 v97, v72, v218
	ds_read_b128 v[216:219], v99 offset:13312
	v_add_f32_e32 v96, v96, v97
	v_add_f32_e32 v47, v96, v47
	s_waitcnt lgkmcnt(7)
	v_mul_f32_e32 v96, v69, v221
	v_mul_f32_e32 v97, v65, v223
	v_fmac_f32_e32 v96, v68, v220
	v_fmac_f32_e32 v97, v64, v222
	ds_read_b128 v[220:223], v99 offset:14336
	v_add_f32_e32 v96, v96, v97
	v_add_f32_e32 v47, v96, v47
	s_waitcnt lgkmcnt(7)
	v_mul_f32_e32 v96, v71, v225
	v_mul_f32_e32 v97, v67, v227
	v_fmac_f32_e32 v96, v70, v224
	v_fmac_f32_e32 v97, v66, v226
	ds_read_b128 v[224:227], v99 offset:15360
	v_add_f32_e32 v96, v96, v97
	v_add_f32_e32 v47, v96, v47
	s_waitcnt lgkmcnt(7)
	v_mul_f32_e32 v96, v93, v197
	v_mul_f32_e32 v97, v91, v199
	v_fmac_f32_e32 v96, v92, v196
	v_fmac_f32_e32 v97, v90, v198
	ds_read_b128 v[196:199], v99 offset:16384
	v_add_f32_e32 v96, v96, v97
	s_waitcnt lgkmcnt(7)
	v_mul_f32_e32 v97, v95, v201
	v_fmac_f32_e32 v97, v94, v200
	v_mul_f32_e32 v174, v89, v203
	v_fmac_f32_e32 v174, v88, v202
	ds_read_b128 v[200:203], v99 offset:17408
	v_add_f32_e32 v96, 0, v96
	v_add_f32_e32 v97, v97, v174
	v_add_f32_e32 v96, v96, v97
	s_waitcnt lgkmcnt(7)
; #define LAS __attribute__((address_space(3)))
; template <int MODE, bool SB  > DI void norm_phase(const Params& P, const Frame& F, int L, const void* src_, const float* gain, bool combine) {
;     ...
;             for (int q = 0; q < 16; ++q) { float t = 0.f;
; #pragma unroll
;                 for (int j = 0; j < 8; ++j) { const f32x4 w = *(const LAS f32x4*)(F.lds + (size_t)(q * D + 256 * j + 4 * F.lane) * 4); t += (v[j][0] * w[0] + v[j][1] * w[1]) + (v[j][2] * w[2] + v[j][3] * w[3]); }
;                 s[q] = t; if ((q & 3) == 3) asm volatile("" ::: "memory"); }
	v_mul_f32_e32 v97, v85, v205
	v_fmac_f32_e32 v97, v84, v204
	v_mul_f32_e32 v170, v83, v207
	v_fmac_f32_e32 v170, v82, v206
	ds_read_b128 v[204:207], v99 offset:18432
	v_add_f32_e32 v97, v97, v170
	v_add_f32_e32 v96, v96, v97
	s_waitcnt lgkmcnt(7)
	v_mul_f32_e32 v97, v87, v209
	v_fmac_f32_e32 v97, v86, v208
	v_mul_f32_e32 v174, v79, v211
	v_fmac_f32_e32 v174, v78, v210
	ds_read_b128 v[208:211], v99 offset:19456
	v_add_f32_e32 v97, v97, v174
	v_add_f32_e32 v96, v96, v97
	s_waitcnt lgkmcnt(7)
	v_mul_f32_e32 v97, v77, v213
	v_fmac_f32_e32 v97, v76, v212
	v_mul_f32_e32 v170, v75, v215
	v_fmac_f32_e32 v170, v74, v214
	ds_read_b128 v[212:215], v99 offset:20480
	v_add_f32_e32 v97, v97, v170
	v_add_f32_e32 v96, v96, v97
	s_waitcnt lgkmcnt(7)
	v_mul_f32_e32 v97, v81, v217
	v_fmac_f32_e32 v97, v80, v216
	v_mul_f32_e32 v174, v73, v219
	v_fmac_f32_e32 v174, v72, v218
	ds_read_b128 v[216:219], v99 offset:21504
	v_add_f32_e32 v97, v97, v174
	v_add_f32_e32 v96, v96, v97
	s_waitcnt lgkmcnt(7)
	v_mul_f32_e32 v97, v69, v221
	v_fmac_f32_e32 v97, v68, v220
	v_mul_f32_e32 v170, v65, v223
	v_fmac_f32_e32 v170, v64, v222
	ds_read_b128 v[220:223], v99 offset:22528
	v_add_f32_e32 v97, v97, v170
	v_add_f32_e32 v96, v96, v97
	s_waitcnt lgkmcnt(7)
	v_mul_f32_e32 v97, v71, v225
	v_fmac_f32_e32 v97, v70, v224
	v_mul_f32_e32 v174, v67, v227
	v_fmac_f32_e32 v174, v66, v226
	ds_read_b128 v[224:227], v99 offset:23552
	v_add_f32_e32 v97, v97, v174
	v_add_f32_e32 v96, v96, v97
	s_waitcnt lgkmcnt(7)
	v_mul_f32_e32 v97, v93, v197
	v_fmac_f32_e32 v97, v92, v196
	v_mul_f32_e32 v170, v91, v199
	v_fmac_f32_e32 v170, v90, v198
	ds_read_b128 v[196:199], v99 offset:24576
	s_waitcnt lgkmcnt(7)
	v_mul_f32_e32 v175, v95, v201
	v_add_f32_e32 v97, v97, v170
	v_fmac_f32_e32 v175, v94, v200
	v_mul_f32_e32 v174, v89, v203
	v_fmac_f32_e32 v174, v88, v202
	ds_read_b128 v[200:203], v99 offset:25600
	v_add_f32_e32 v97, 0, v97
	v_add_f32_e32 v174, v175, v174
	v_add_f32_e32 v97, v97, v174
	s_waitcnt lgkmcnt(7)
	v_mul_f32_e32 v171, v85, v205
	v_fmac_f32_e32 v171, v84, v204
	v_mul_f32_e32 v170, v83, v207
	v_fmac_f32_e32 v170, v82, v206
	ds_read_b128 v[204:207], v99 offset:26624
	v_add_f32_e32 v170, v171, v170
	s_waitcnt lgkmcnt(7)
	v_mul_f32_e32 v175, v87, v209
	v_add_f32_e32 v97, v97, v170
	v_fmac_f32_e32 v175, v86, v208
	v_mul_f32_e32 v174, v79, v211
	v_fmac_f32_e32 v174, v78, v210
	ds_read_b128 v[208:211], v99 offset:27648
	v_add_f32_e32 v174, v175, v174
	v_add_f32_e32 v97, v97, v174
	s_waitcnt lgkmcnt(7)
	v_mul_f32_e32 v171, v77, v213
	v_fmac_f32_e32 v171, v76, v212
	v_mul_f32_e32 v170, v75, v215
	v_fmac_f32_e32 v170, v74, v214
	ds_read_b128 v[212:215], v99 offset:28672
	v_add_f32_e32 v170, v171, v170
	s_waitcnt lgkmcnt(7)
	v_mul_f32_e32 v175, v81, v217
	v_add_f32_e32 v97, v97, v170
	v_fmac_f32_e32 v175, v80, v216
	v_mul_f32_e32 v174, v73, v219
	v_fmac_f32_e32 v174, v72, v218
	ds_read_b128 v[216:219], v99 offset:29696
	v_add_f32_e32 v174, v175, v174
	v_add_f32_e32 v97, v97, v174
	s_waitcnt lgkmcnt(7)
	v_mul_f32_e32 v171, v69, v221
	v_fmac_f32_e32 v171, v68, v220
	v_mul_f32_e32 v170, v65, v223
	v_fmac_f32_e32 v170, v64, v222
	ds_read_b128 v[220:223], v99 offset:30720
	v_add_f32_e32 v170, v171, v170
	s_waitcnt lgkmcnt(7)
	v_mul_f32_e32 v175, v71, v225
	v_add_f32_e32 v97, v97, v170
	v_fmac_f32_e32 v175, v70, v224
	v_mul_f32_e32 v174, v67, v227
	v_fmac_f32_e32 v174, v66, v226
	ds_read_b128 v[224:227], v99 offset:31744
	v_add_f32_e32 v174, v175, v174
	v_add_f32_e32 v97, v97, v174
	s_waitcnt lgkmcnt(7)
	v_mul_f32_e32 v171, v93, v197
	v_fmac_f32_e32 v171, v92, v196
	v_mul_f32_e32 v170, v91, v199
	v_fmac_f32_e32 v170, v90, v198
	ds_read_b128 v[196:199], v99 offset:32768
	v_add_f32_e32 v170, v171, v170
	s_waitcnt lgkmcnt(7)
	v_mul_f32_e32 v175, v95, v201
	v_add_f32_e32 v178, 0, v170
	v_fmac_f32_e32 v175, v94, v200
	v_mul_f32_e32 v174, v89, v203
	v_fmac_f32_e32 v174, v88, v202
	ds_read_b128 v[200:203], v99 offset:33792
	v_add_f32_e32 v174, v175, v174
	v_add_f32_e32 v178, v178, v174
	s_waitcnt lgkmcnt(7)
	v_mul_f32_e32 v171, v85, v205
	v_fmac_f32_e32 v171, v84, v204
	v_mul_f32_e32 v170, v83, v207
	v_fmac_f32_e32 v170, v82, v206
	ds_read_b128 v[204:207], v99 offset:34816
	v_add_f32_e32 v170, v171, v170
	s_waitcnt lgkmcnt(7)
	v_mul_f32_e32 v175, v87, v209
	v_add_f32_e32 v178, v178, v170
	v_fmac_f32_e32 v175, v86, v208
	v_mul_f32_e32 v174, v79, v211
	v_fmac_f32_e32 v174, v78, v210
	ds_read_b128 v[208:211], v99 offset:35840
	v_add_f32_e32 v174, v175, v174
	v_add_f32_e32 v178, v178, v174
	s_waitcnt lgkmcnt(7)
	v_mul_f32_e32 v171, v77, v213
	v_fmac_f32_e32 v171, v76, v212
	v_mul_f32_e32 v170, v75, v215
	v_fmac_f32_e32 v170, v74, v214
	ds_read_b128 v[212:215], v99 offset:36864
	v_add_f32_e32 v170, v171, v170
	s_waitcnt lgkmcnt(7)
	v_mul_f32_e32 v175, v81, v217
	v_add_f32_e32 v178, v178, v170
	v_fmac_f32_e32 v175, v80, v216
	v_mul_f32_e32 v174, v73, v219
	v_fmac_f32_e32 v174, v72, v218
	ds_read_b128 v[216:219], v99 offset:37888
	v_add_f32_e32 v174, v175, v174
	v_add_f32_e32 v178, v178, v174
	s_waitcnt lgkmcnt(7)
	v_mul_f32_e32 v171, v69, v221
	v_fmac_f32_e32 v171, v68, v220
	v_mul_f32_e32 v170, v65, v223
	v_fmac_f32_e32 v170, v64, v222
	ds_read_b128 v[220:223], v99 offset:38912
	v_add_f32_e32 v170, v171, v170
	s_waitcnt lgkmcnt(7)
	v_mul_f32_e32 v171, v71, v225
	v_fmac_f32_e32 v171, v70, v224
	v_mul_f32_e32 v177, v67, v227
	v_fmac_f32_e32 v177, v66, v226
	ds_read_b128 v[224:227], v99 offset:39936
	v_add_f32_e32 v170, v178, v170
	v_add_f32_e32 v171, v171, v177
	v_add_f32_e32 v170, v170, v171
	s_waitcnt lgkmcnt(7)
	v_mul_f32_e32 v171, v93, v197
	v_fmac_f32_e32 v171, v92, v196
	v_mul_f32_e32 v172, v91, v199
	v_fmac_f32_e32 v172, v90, v198
	ds_read_b128 v[196:199], v99 offset:40960
	s_waitcnt lgkmcnt(7)
; #define LAS __attribute__((address_space(3)))
; template <int MODE, bool SB  > DI void norm_phase(const Params& P, const Frame& F, int L, const void* src_, const float* gain, bool combine) {
;     ...
;             for (int q = 0; q < 16; ++q) { float t = 0.f;
; #pragma unroll
;                 for (int j = 0; j < 8; ++j) { const f32x4 w = *(const LAS f32x4*)(F.lds + (size_t)(q * D + 256 * j + 4 * F.lane) * 4); t += (v[j][0] * w[0] + v[j][1] * w[1]) + (v[j][2] * w[2] + v[j][3] * w[3]); }
;                 s[q] = t; if ((q & 3) == 3) asm volatile("" ::: "memory"); }
	v_mul_f32_e32 v177, v95, v201
	v_add_f32_e32 v171, v171, v172
	v_fmac_f32_e32 v177, v94, v200
	v_mul_f32_e32 v176, v89, v203
	v_fmac_f32_e32 v176, v88, v202
	ds_read_b128 v[200:203], v99 offset:41984
	v_add_f32_e32 v171, 0, v171
	v_add_f32_e32 v176, v177, v176
	v_add_f32_e32 v171, v171, v176
	s_waitcnt lgkmcnt(7)
	v_mul_f32_e32 v173, v85, v205
	v_fmac_f32_e32 v173, v84, v204
	v_mul_f32_e32 v172, v83, v207
	v_fmac_f32_e32 v172, v82, v206
	ds_read_b128 v[204:207], v99 offset:43008
	v_add_f32_e32 v172, v173, v172
	s_waitcnt lgkmcnt(7)
	v_mul_f32_e32 v177, v87, v209
	v_add_f32_e32 v171, v171, v172
	v_fmac_f32_e32 v177, v86, v208
	v_mul_f32_e32 v176, v79, v211
	v_fmac_f32_e32 v176, v78, v210
	ds_read_b128 v[208:211], v99 offset:44032
	v_add_f32_e32 v176, v177, v176
	v_add_f32_e32 v171, v171, v176
	s_waitcnt lgkmcnt(7)
	v_mul_f32_e32 v173, v77, v213
	v_fmac_f32_e32 v173, v76, v212
	v_mul_f32_e32 v172, v75, v215
	v_fmac_f32_e32 v172, v74, v214
	ds_read_b128 v[212:215], v99 offset:45056
	v_add_f32_e32 v172, v173, v172
	s_waitcnt lgkmcnt(7)
	v_mul_f32_e32 v177, v81, v217
	v_add_f32_e32 v171, v171, v172
	v_fmac_f32_e32 v177, v80, v216
	v_mul_f32_e32 v176, v73, v219
	v_fmac_f32_e32 v176, v72, v218
	ds_read_b128 v[216:219], v99 offset:46080
	v_add_f32_e32 v176, v177, v176
	v_add_f32_e32 v171, v171, v176
	s_waitcnt lgkmcnt(7)
	v_mul_f32_e32 v173, v69, v221
	v_fmac_f32_e32 v173, v68, v220
	v_mul_f32_e32 v172, v65, v223
	v_fmac_f32_e32 v172, v64, v222
	ds_read_b128 v[220:223], v99 offset:47104
	v_add_f32_e32 v172, v173, v172
	s_waitcnt lgkmcnt(7)
	v_mul_f32_e32 v177, v71, v225
	v_add_f32_e32 v171, v171, v172
	v_fmac_f32_e32 v177, v70, v224
	v_mul_f32_e32 v176, v67, v227
	v_fmac_f32_e32 v176, v66, v226
	ds_read_b128 v[224:227], v99 offset:48128
	v_add_f32_e32 v176, v177, v176
	v_add_f32_e32 v171, v171, v176
	s_waitcnt lgkmcnt(7)
	v_mul_f32_e32 v173, v93, v197
	v_fmac_f32_e32 v173, v92, v196
	v_mul_f32_e32 v172, v91, v199
	v_fmac_f32_e32 v172, v90, v198
	ds_read_b128 v[196:199], v99 offset:49152
	v_add_f32_e32 v172, v173, v172
	s_waitcnt lgkmcnt(7)
	v_mul_f32_e32 v177, v95, v201
	v_add_f32_e32 v180, 0, v172
	v_fmac_f32_e32 v177, v94, v200
	v_mul_f32_e32 v176, v89, v203
	v_fmac_f32_e32 v176, v88, v202
	ds_read_b128 v[200:203], v99 offset:50176
	v_add_f32_e32 v176, v177, v176
	v_add_f32_e32 v180, v180, v176
	s_waitcnt lgkmcnt(7)
	v_mul_f32_e32 v173, v85, v205
	v_fmac_f32_e32 v173, v84, v204
	v_mul_f32_e32 v172, v83, v207
	v_fmac_f32_e32 v172, v82, v206
	ds_read_b128 v[204:207], v99 offset:51200
	v_add_f32_e32 v172, v173, v172
	s_waitcnt lgkmcnt(7)
	v_mul_f32_e32 v177, v87, v209
	v_add_f32_e32 v180, v180, v172
	v_fmac_f32_e32 v177, v86, v208
	v_mul_f32_e32 v176, v79, v211
	v_fmac_f32_e32 v176, v78, v210
	ds_read_b128 v[208:211], v99 offset:52224
	v_add_f32_e32 v176, v177, v176
	v_add_f32_e32 v180, v180, v176
	s_waitcnt lgkmcnt(7)
	v_mul_f32_e32 v173, v77, v213
	v_fmac_f32_e32 v173, v76, v212
	v_mul_f32_e32 v172, v75, v215
	v_fmac_f32_e32 v172, v74, v214
	ds_read_b128 v[212:215], v99 offset:53248
	v_add_f32_e32 v172, v173, v172
	s_waitcnt lgkmcnt(7)
	v_mul_f32_e32 v177, v81, v217
	v_add_f32_e32 v180, v180, v172
	v_fmac_f32_e32 v177, v80, v216
	v_mul_f32_e32 v176, v73, v219
	v_fmac_f32_e32 v176, v72, v218
	ds_read_b128 v[216:219], v99 offset:54272
	v_add_f32_e32 v176, v177, v176
	v_add_f32_e32 v180, v180, v176
	s_waitcnt lgkmcnt(7)
	v_mul_f32_e32 v173, v69, v221
	v_fmac_f32_e32 v173, v68, v220
	v_mul_f32_e32 v172, v65, v223
	v_fmac_f32_e32 v172, v64, v222
	ds_read_b128 v[220:223], v99 offset:55296
	v_add_f32_e32 v172, v173, v172
	s_waitcnt lgkmcnt(7)
	v_mul_f32_e32 v173, v71, v225
	v_fmac_f32_e32 v173, v70, v224
	v_mul_f32_e32 v179, v67, v227
	v_fmac_f32_e32 v179, v66, v226
	ds_read_b128 v[224:227], v99 offset:56320
	v_add_f32_e32 v172, v180, v172
	v_add_f32_e32 v173, v173, v179
	v_add_f32_e32 v172, v172, v173
	s_waitcnt lgkmcnt(7)
	v_mul_f32_e32 v173, v93, v197
	v_fmac_f32_e32 v173, v92, v196
	v_mul_f32_e32 v174, v91, v199
	v_fmac_f32_e32 v174, v90, v198
	ds_read_b128 v[196:199], v99 offset:57344
	s_waitcnt lgkmcnt(7)
	v_mul_f32_e32 v179, v95, v201
	v_add_f32_e32 v173, v173, v174
	v_fmac_f32_e32 v179, v94, v200
	v_mul_f32_e32 v178, v89, v203
	v_fmac_f32_e32 v178, v88, v202
	ds_read_b128 v[200:203], v99 offset:58368
	v_add_f32_e32 v173, 0, v173
	v_add_f32_e32 v178, v179, v178
	v_add_f32_e32 v173, v173, v178
	s_waitcnt lgkmcnt(7)
	v_mul_f32_e32 v175, v85, v205
	v_fmac_f32_e32 v175, v84, v204
	v_mul_f32_e32 v174, v83, v207
	v_fmac_f32_e32 v174, v82, v206
	ds_read_b128 v[204:207], v99 offset:59392
	v_add_f32_e32 v174, v175, v174
	s_waitcnt lgkmcnt(7)
	v_mul_f32_e32 v179, v87, v209
	v_add_f32_e32 v173, v173, v174
	v_fmac_f32_e32 v179, v86, v208
	v_mul_f32_e32 v178, v79, v211
	v_fmac_f32_e32 v178, v78, v210
	ds_read_b128 v[208:211], v99 offset:60416
	v_add_f32_e32 v178, v179, v178
	v_add_f32_e32 v173, v173, v178
	s_waitcnt lgkmcnt(7)
	v_mul_f32_e32 v175, v77, v213
	v_fmac_f32_e32 v175, v76, v212
	v_mul_f32_e32 v174, v75, v215
	v_fmac_f32_e32 v174, v74, v214
	ds_read_b128 v[212:215], v99 offset:61440
	v_add_f32_e32 v174, v175, v174
	s_waitcnt lgkmcnt(7)
	v_mul_f32_e32 v179, v81, v217
	v_add_f32_e32 v173, v173, v174
	v_fmac_f32_e32 v179, v80, v216
	v_mul_f32_e32 v178, v73, v219
	v_fmac_f32_e32 v178, v72, v218
	ds_read_b128 v[216:219], v99 offset:62464
	v_add_f32_e32 v178, v179, v178
	v_add_f32_e32 v173, v173, v178
	s_waitcnt lgkmcnt(7)
	v_mul_f32_e32 v175, v69, v221
	v_fmac_f32_e32 v175, v68, v220
	v_mul_f32_e32 v174, v65, v223
	v_fmac_f32_e32 v174, v64, v222
	ds_read_b128 v[220:223], v99 offset:63488
	v_add_f32_e32 v174, v175, v174
	s_waitcnt lgkmcnt(7)
; #define LAS __attribute__((address_space(3)))
; template <int MODE, bool SB  > DI void norm_phase(const Params& P, const Frame& F, int L, const void* src_, const float* gain, bool combine) {
;     ...
;             for (int q = 0; q < 16; ++q) { float t = 0.f;
; #pragma unroll
;                 for (int j = 0; j < 8; ++j) { const f32x4 w = *(const LAS f32x4*)(F.lds + (size_t)(q * D + 256 * j + 4 * F.lane) * 4); t += (v[j][0] * w[0] + v[j][1] * w[1]) + (v[j][2] * w[2] + v[j][3] * w[3]); }
;                 s[q] = t; if ((q & 3) == 3) asm volatile("" ::: "memory"); }
	v_mul_f32_e32 v179, v71, v225
	v_add_f32_e32 v173, v173, v174
	v_fmac_f32_e32 v179, v70, v224
	v_mul_f32_e32 v178, v67, v227
	v_fmac_f32_e32 v178, v66, v226
	ds_read_b128 v[224:227], v99 offset:64512
	v_add_f32_e32 v178, v179, v178
	v_add_f32_e32 v173, v173, v178
	s_waitcnt lgkmcnt(7)
	v_mul_f32_e32 v175, v93, v197
	v_fmac_f32_e32 v175, v92, v196
	v_mul_f32_e32 v174, v91, v199
	v_fmac_f32_e32 v174, v90, v198
	ds_read_b128 v[196:199], v100
	v_add_f32_e32 v174, v175, v174
	s_waitcnt lgkmcnt(7)
	v_mul_f32_e32 v179, v95, v201
	v_add_f32_e32 v182, 0, v174
	v_fmac_f32_e32 v179, v94, v200
	v_mul_f32_e32 v178, v89, v203
	v_fmac_f32_e32 v178, v88, v202
	ds_read_b128 v[200:203], v101
	v_add_f32_e32 v178, v179, v178
	v_add_f32_e32 v182, v182, v178
	s_waitcnt lgkmcnt(7)
	v_mul_f32_e32 v175, v85, v205
	v_fmac_f32_e32 v175, v84, v204
	v_mul_f32_e32 v174, v83, v207
	v_fmac_f32_e32 v174, v82, v206
	ds_read_b128 v[204:207], v102
	v_add_f32_e32 v174, v175, v174
	s_waitcnt lgkmcnt(7)
	v_mul_f32_e32 v179, v87, v209
	v_add_f32_e32 v182, v182, v174
	v_fmac_f32_e32 v179, v86, v208
	v_mul_f32_e32 v178, v79, v211
	v_fmac_f32_e32 v178, v78, v210
	ds_read_b128 v[208:211], v103
	v_add_f32_e32 v178, v179, v178
	v_add_f32_e32 v182, v182, v178
	s_waitcnt lgkmcnt(7)
	v_mul_f32_e32 v175, v77, v213
	v_fmac_f32_e32 v175, v76, v212
	v_mul_f32_e32 v174, v75, v215
	v_fmac_f32_e32 v174, v74, v214
	ds_read_b128 v[212:215], v104
	v_add_f32_e32 v174, v175, v174
	s_waitcnt lgkmcnt(7)
	v_mul_f32_e32 v179, v81, v217
	v_add_f32_e32 v182, v182, v174
	v_fmac_f32_e32 v179, v80, v216
	v_mul_f32_e32 v178, v73, v219
	v_fmac_f32_e32 v178, v72, v218
	ds_read_b128 v[216:219], v105
	v_add_f32_e32 v178, v179, v178
	v_add_f32_e32 v182, v182, v178
	s_waitcnt lgkmcnt(7)
	v_mul_f32_e32 v175, v69, v221
	v_fmac_f32_e32 v175, v68, v220
	v_mul_f32_e32 v174, v65, v223
	v_fmac_f32_e32 v174, v64, v222
	ds_read_b128 v[220:223], v106
	v_add_f32_e32 v174, v175, v174
	s_waitcnt lgkmcnt(7)
	v_mul_f32_e32 v175, v71, v225
	v_fmac_f32_e32 v175, v70, v224
	v_mul_f32_e32 v181, v67, v227
	v_fmac_f32_e32 v181, v66, v226
	ds_read_b128 v[224:227], v107
	v_add_f32_e32 v174, v182, v174
	v_add_f32_e32 v175, v175, v181
	v_add_f32_e32 v174, v174, v175
	s_waitcnt lgkmcnt(7)
	v_mul_f32_e32 v175, v93, v197
	v_fmac_f32_e32 v175, v92, v196
	v_mul_f32_e32 v176, v91, v199
	v_fmac_f32_e32 v176, v90, v198
	ds_read_b128 v[196:199], v108
	s_waitcnt lgkmcnt(7)
	v_mul_f32_e32 v181, v95, v201
	v_add_f32_e32 v175, v175, v176
	v_fmac_f32_e32 v181, v94, v200
	v_mul_f32_e32 v180, v89, v203
	v_fmac_f32_e32 v180, v88, v202
	ds_read_b128 v[200:203], v109
	v_add_f32_e32 v175, 0, v175
	v_add_f32_e32 v180, v181, v180
	v_add_f32_e32 v175, v175, v180
	s_waitcnt lgkmcnt(7)
	v_mul_f32_e32 v177, v85, v205
	v_fmac_f32_e32 v177, v84, v204
	v_mul_f32_e32 v176, v83, v207
	v_fmac_f32_e32 v176, v82, v206
	ds_read_b128 v[204:207], v110
	v_add_f32_e32 v176, v177, v176
	s_waitcnt lgkmcnt(7)
	v_mul_f32_e32 v181, v87, v209
	v_add_f32_e32 v175, v175, v176
	v_fmac_f32_e32 v181, v86, v208
	v_mul_f32_e32 v180, v79, v211
	v_fmac_f32_e32 v180, v78, v210
	ds_read_b128 v[208:211], v111
	v_add_f32_e32 v180, v181, v180
	v_add_f32_e32 v175, v175, v180
	s_waitcnt lgkmcnt(7)
	v_mul_f32_e32 v177, v77, v213
	v_fmac_f32_e32 v177, v76, v212
	v_mul_f32_e32 v176, v75, v215
	v_fmac_f32_e32 v176, v74, v214
	ds_read_b128 v[212:215], v112
	v_add_f32_e32 v176, v177, v176
	s_waitcnt lgkmcnt(7)
	v_mul_f32_e32 v181, v81, v217
	v_add_f32_e32 v175, v175, v176
	v_fmac_f32_e32 v181, v80, v216
	v_mul_f32_e32 v180, v73, v219
	v_fmac_f32_e32 v180, v72, v218
	ds_read_b128 v[216:219], v113
	v_add_f32_e32 v180, v181, v180
	v_add_f32_e32 v175, v175, v180
	s_waitcnt lgkmcnt(7)
	v_mul_f32_e32 v177, v69, v221
	v_fmac_f32_e32 v177, v68, v220
	v_mul_f32_e32 v176, v65, v223
	v_fmac_f32_e32 v176, v64, v222
	ds_read_b128 v[220:223], v114
	v_add_f32_e32 v176, v177, v176
	s_waitcnt lgkmcnt(7)
	v_mul_f32_e32 v181, v71, v225
	v_add_f32_e32 v175, v175, v176
	v_fmac_f32_e32 v181, v70, v224
	v_mul_f32_e32 v180, v67, v227
	v_fmac_f32_e32 v180, v66, v226
	ds_read_b128 v[224:227], v115
	v_add_f32_e32 v180, v181, v180
	v_add_f32_e32 v175, v175, v180
	s_waitcnt lgkmcnt(7)
	v_mul_f32_e32 v177, v93, v197
	v_fmac_f32_e32 v177, v92, v196
	v_mul_f32_e32 v176, v91, v199
	v_fmac_f32_e32 v176, v90, v198
	ds_read_b128 v[196:199], v116
	v_add_f32_e32 v176, v177, v176
	s_waitcnt lgkmcnt(7)
	v_mul_f32_e32 v181, v95, v201
	v_add_f32_e32 v184, 0, v176
	v_fmac_f32_e32 v181, v94, v200
	v_mul_f32_e32 v180, v89, v203
	v_fmac_f32_e32 v180, v88, v202
	ds_read_b128 v[200:203], v117
	v_add_f32_e32 v180, v181, v180
	v_add_f32_e32 v184, v184, v180
	s_waitcnt lgkmcnt(7)
	v_mul_f32_e32 v177, v85, v205
	v_fmac_f32_e32 v177, v84, v204
	v_mul_f32_e32 v176, v83, v207
	v_fmac_f32_e32 v176, v82, v206
	ds_read_b128 v[204:207], v118
	v_add_f32_e32 v176, v177, v176
	s_waitcnt lgkmcnt(7)
	v_mul_f32_e32 v181, v87, v209
	v_add_f32_e32 v184, v184, v176
	v_fmac_f32_e32 v181, v86, v208
	v_mul_f32_e32 v180, v79, v211
	v_fmac_f32_e32 v180, v78, v210
	ds_read_b128 v[208:211], v119
	v_add_f32_e32 v180, v181, v180
	v_add_f32_e32 v184, v184, v180
	s_waitcnt lgkmcnt(7)
	v_mul_f32_e32 v177, v77, v213
	v_fmac_f32_e32 v177, v76, v212
	v_mul_f32_e32 v176, v75, v215
	v_fmac_f32_e32 v176, v74, v214
	ds_read_b128 v[212:215], v120
	v_add_f32_e32 v176, v177, v176
	s_waitcnt lgkmcnt(7)
	v_mul_f32_e32 v181, v81, v217
	v_add_f32_e32 v184, v184, v176
	v_fmac_f32_e32 v181, v80, v216
	v_mul_f32_e32 v180, v73, v219
	v_fmac_f32_e32 v180, v72, v218
	ds_read_b128 v[216:219], v121
	v_add_f32_e32 v180, v181, v180
	v_add_f32_e32 v184, v184, v180
	s_waitcnt lgkmcnt(7)
; #define LAS __attribute__((address_space(3)))
; template <int MODE, bool SB  > DI void norm_phase(const Params& P, const Frame& F, int L, const void* src_, const float* gain, bool combine) {
;     ...
;             for (int q = 0; q < 16; ++q) { float t = 0.f;
; #pragma unroll
;                 for (int j = 0; j < 8; ++j) { const f32x4 w = *(const LAS f32x4*)(F.lds + (size_t)(q * D + 256 * j + 4 * F.lane) * 4); t += (v[j][0] * w[0] + v[j][1] * w[1]) + (v[j][2] * w[2] + v[j][3] * w[3]); }
;                 s[q] = t; if ((q & 3) == 3) asm volatile("" ::: "memory"); }
	v_mul_f32_e32 v177, v69, v221
	v_fmac_f32_e32 v177, v68, v220
	v_mul_f32_e32 v176, v65, v223
	v_fmac_f32_e32 v176, v64, v222
	ds_read_b128 v[220:223], v122
	v_add_f32_e32 v176, v177, v176
	s_waitcnt lgkmcnt(7)
	v_mul_f32_e32 v177, v71, v225
	v_mul_f32_e32 v183, v67, v227
	v_fmac_f32_e32 v177, v70, v224
	v_fmac_f32_e32 v183, v66, v226
	ds_read_b128 v[224:227], v123
	v_add_f32_e32 v176, v184, v176
	v_add_f32_e32 v177, v177, v183
	v_add_f32_e32 v176, v176, v177
	s_waitcnt lgkmcnt(7)
	v_mul_f32_e32 v177, v93, v197
	v_fmac_f32_e32 v177, v92, v196
	v_mul_f32_e32 v178, v91, v199
	s_waitcnt lgkmcnt(6)
	v_mul_f32_e32 v183, v95, v201
	v_fmac_f32_e32 v178, v90, v198
	ds_read_b128 v[196:199], v124
	v_fmac_f32_e32 v183, v94, v200
	v_mul_f32_e32 v182, v89, v203
	v_add_f32_e32 v177, v177, v178
	v_fmac_f32_e32 v182, v88, v202
	ds_read_b128 v[200:203], v125
	v_add_f32_e32 v177, 0, v177
	v_add_f32_e32 v182, v183, v182
	v_add_f32_e32 v177, v177, v182
	s_waitcnt lgkmcnt(7)
	v_mul_f32_e32 v179, v85, v205
	v_fmac_f32_e32 v179, v84, v204
	v_mul_f32_e32 v178, v83, v207
	v_fmac_f32_e32 v178, v82, v206
	ds_read_b128 v[204:207], v126
	s_waitcnt lgkmcnt(7)
	v_mul_f32_e32 v183, v87, v209
	v_add_f32_e32 v178, v179, v178
	v_fmac_f32_e32 v183, v86, v208
	v_mul_f32_e32 v182, v79, v211
	v_add_f32_e32 v177, v177, v178
	v_fmac_f32_e32 v182, v78, v210
	ds_read_b128 v[208:211], v127
	v_add_f32_e32 v182, v183, v182
	v_add_f32_e32 v177, v177, v182
	s_waitcnt lgkmcnt(7)
	v_mul_f32_e32 v179, v77, v213
	v_fmac_f32_e32 v179, v76, v212
	v_mul_f32_e32 v178, v75, v215
	v_fmac_f32_e32 v178, v74, v214
	ds_read_b128 v[212:215], v128
	s_waitcnt lgkmcnt(7)
	v_mul_f32_e32 v183, v81, v217
	v_add_f32_e32 v178, v179, v178
	v_fmac_f32_e32 v183, v80, v216
	v_mul_f32_e32 v182, v73, v219
	v_add_f32_e32 v177, v177, v178
	v_fmac_f32_e32 v182, v72, v218
	ds_read_b128 v[216:219], v129
	v_add_f32_e32 v182, v183, v182
	v_add_f32_e32 v177, v177, v182
	s_waitcnt lgkmcnt(7)
	v_mul_f32_e32 v179, v69, v221
	v_fmac_f32_e32 v179, v68, v220
	v_mul_f32_e32 v178, v65, v223
	v_fmac_f32_e32 v178, v64, v222
	ds_read_b128 v[220:223], v130
	s_waitcnt lgkmcnt(7)
	v_mul_f32_e32 v183, v71, v225
	v_add_f32_e32 v178, v179, v178
	v_fmac_f32_e32 v183, v70, v224
	v_mul_f32_e32 v182, v67, v227
	v_add_f32_e32 v177, v177, v178
	v_fmac_f32_e32 v182, v66, v226
	ds_read_b128 v[224:227], v131
	v_add_f32_e32 v182, v183, v182
	v_add_f32_e32 v177, v177, v182
	s_waitcnt lgkmcnt(7)
	v_mul_f32_e32 v179, v93, v197
	v_fmac_f32_e32 v179, v92, v196
	v_mul_f32_e32 v178, v91, v199
	v_fmac_f32_e32 v178, v90, v198
	ds_read_b128 v[196:199], v132
	s_waitcnt lgkmcnt(7)
	v_mul_f32_e32 v183, v95, v201
	v_add_f32_e32 v178, v179, v178
	v_fmac_f32_e32 v183, v94, v200
	v_mul_f32_e32 v182, v89, v203
	v_add_f32_e32 v186, 0, v178
	v_fmac_f32_e32 v182, v88, v202
	ds_read_b128 v[200:203], v133
	v_add_f32_e32 v182, v183, v182
	v_add_f32_e32 v186, v186, v182
	s_waitcnt lgkmcnt(7)
	v_mul_f32_e32 v179, v85, v205
	v_fmac_f32_e32 v179, v84, v204
	v_mul_f32_e32 v178, v83, v207
	v_fmac_f32_e32 v178, v82, v206
	ds_read_b128 v[204:207], v134
	s_waitcnt lgkmcnt(7)
	v_mul_f32_e32 v183, v87, v209
	v_add_f32_e32 v178, v179, v178
	v_fmac_f32_e32 v183, v86, v208
	v_mul_f32_e32 v182, v79, v211
	v_add_f32_e32 v186, v186, v178
	v_fmac_f32_e32 v182, v78, v210
	ds_read_b128 v[208:211], v135
	v_add_f32_e32 v182, v183, v182
	v_add_f32_e32 v186, v186, v182
	s_waitcnt lgkmcnt(7)
	v_mul_f32_e32 v179, v77, v213
	v_fmac_f32_e32 v179, v76, v212
	v_mul_f32_e32 v178, v75, v215
	v_fmac_f32_e32 v178, v74, v214
	ds_read_b128 v[212:215], v136
	s_waitcnt lgkmcnt(7)
	v_mul_f32_e32 v183, v81, v217
	v_add_f32_e32 v178, v179, v178
	v_fmac_f32_e32 v183, v80, v216
	v_mul_f32_e32 v182, v73, v219
	v_add_f32_e32 v186, v186, v178
	v_fmac_f32_e32 v182, v72, v218
	ds_read_b128 v[216:219], v137
	v_add_f32_e32 v182, v183, v182
	v_add_f32_e32 v186, v186, v182
	s_waitcnt lgkmcnt(7)
	v_mul_f32_e32 v179, v69, v221
	v_fmac_f32_e32 v179, v68, v220
	v_mul_f32_e32 v178, v65, v223
	v_fmac_f32_e32 v178, v64, v222
	ds_read_b128 v[220:223], v138
	s_waitcnt lgkmcnt(7)
	v_mul_f32_e32 v183, v71, v225
	v_add_f32_e32 v178, v179, v178
	v_fmac_f32_e32 v183, v70, v224
	v_mul_f32_e32 v182, v67, v227
	v_add_f32_e32 v186, v186, v178
	v_fmac_f32_e32 v182, v66, v226
	ds_read_b128 v[224:227], v139
	v_add_f32_e32 v182, v183, v182
	v_add_f32_e32 v186, v186, v182
	s_waitcnt lgkmcnt(7)
	v_mul_f32_e32 v179, v93, v197
	v_fmac_f32_e32 v179, v92, v196
	v_mul_f32_e32 v178, v91, v199
	v_fmac_f32_e32 v178, v90, v198
	ds_read_b128 v[196:199], v140
	s_waitcnt lgkmcnt(7)
	v_mul_f32_e32 v183, v95, v201
	v_add_f32_e32 v178, v179, v178
	v_fmac_f32_e32 v183, v94, v200
	v_mul_f32_e32 v182, v89, v203
	v_add_f32_e32 v187, 0, v178
	v_fmac_f32_e32 v182, v88, v202
	ds_read_b128 v[200:203], v141
	v_add_f32_e32 v182, v183, v182
	v_add_f32_e32 v187, v187, v182
	s_waitcnt lgkmcnt(7)
	v_mul_f32_e32 v179, v85, v205
	v_fmac_f32_e32 v179, v84, v204
	v_mul_f32_e32 v178, v83, v207
	v_fmac_f32_e32 v178, v82, v206
	ds_read_b128 v[204:207], v142
	s_waitcnt lgkmcnt(7)
	v_mul_f32_e32 v183, v87, v209
	v_add_f32_e32 v178, v179, v178
	v_fmac_f32_e32 v183, v86, v208
	v_mul_f32_e32 v182, v79, v211
	v_add_f32_e32 v187, v187, v178
	v_fmac_f32_e32 v182, v78, v210
	ds_read_b128 v[208:211], v143
	v_add_f32_e32 v182, v183, v182
	v_add_f32_e32 v187, v187, v182
	s_waitcnt lgkmcnt(7)
	v_mul_f32_e32 v179, v77, v213
	v_fmac_f32_e32 v179, v76, v212
	v_mul_f32_e32 v178, v75, v215
	v_fmac_f32_e32 v178, v74, v214
	ds_read_b128 v[212:215], v144
	s_waitcnt lgkmcnt(7)
; #define LAS __attribute__((address_space(3)))
; template <int MODE, bool SB  > DI void norm_phase(const Params& P, const Frame& F, int L, const void* src_, const float* gain, bool combine) {
;     ...
;             for (int q = 0; q < 16; ++q) { float t = 0.f;
; #pragma unroll
;                 for (int j = 0; j < 8; ++j) { const f32x4 w = *(const LAS f32x4*)(F.lds + (size_t)(q * D + 256 * j + 4 * F.lane) * 4); t += (v[j][0] * w[0] + v[j][1] * w[1]) + (v[j][2] * w[2] + v[j][3] * w[3]); }
;                 s[q] = t; if ((q & 3) == 3) asm volatile("" ::: "memory"); }
	v_mul_f32_e32 v183, v81, v217
	v_add_f32_e32 v178, v179, v178
	v_fmac_f32_e32 v183, v80, v216
	v_mul_f32_e32 v182, v73, v219
	v_add_f32_e32 v187, v187, v178
	v_fmac_f32_e32 v182, v72, v218
	ds_read_b128 v[216:219], v145
	v_add_f32_e32 v182, v183, v182
	v_add_f32_e32 v187, v187, v182
	s_waitcnt lgkmcnt(7)
	v_mul_f32_e32 v179, v69, v221
	v_fmac_f32_e32 v179, v68, v220
	v_mul_f32_e32 v178, v65, v223
	v_fmac_f32_e32 v178, v64, v222
	ds_read_b128 v[220:223], v146
	s_waitcnt lgkmcnt(7)
	v_mul_f32_e32 v183, v71, v225
	v_add_f32_e32 v178, v179, v178
	v_fmac_f32_e32 v183, v70, v224
	v_mul_f32_e32 v182, v67, v227
	v_add_f32_e32 v187, v187, v178
	v_fmac_f32_e32 v182, v66, v226
	ds_read_b128 v[224:227], v147
	v_add_f32_e32 v182, v183, v182
	v_add_f32_e32 v187, v187, v182
	s_waitcnt lgkmcnt(7)
	v_mul_f32_e32 v179, v93, v197
	v_fmac_f32_e32 v179, v92, v196
	v_mul_f32_e32 v178, v91, v199
	v_fmac_f32_e32 v178, v90, v198
	ds_read_b128 v[196:199], v148
	s_waitcnt lgkmcnt(7)
	v_mul_f32_e32 v183, v95, v201
	v_add_f32_e32 v178, v179, v178
	v_fmac_f32_e32 v183, v94, v200
	v_mul_f32_e32 v182, v89, v203
	v_add_f32_e32 v188, 0, v178
	v_fmac_f32_e32 v182, v88, v202
	ds_read_b128 v[200:203], v149
	v_add_f32_e32 v182, v183, v182
	v_add_f32_e32 v188, v188, v182
	s_waitcnt lgkmcnt(7)
	v_mul_f32_e32 v179, v85, v205
	v_fmac_f32_e32 v179, v84, v204
	v_mul_f32_e32 v178, v83, v207
	v_fmac_f32_e32 v178, v82, v206
	ds_read_b128 v[204:207], v150
	s_waitcnt lgkmcnt(7)
	v_mul_f32_e32 v183, v87, v209
	v_add_f32_e32 v178, v179, v178
	v_fmac_f32_e32 v183, v86, v208
	v_mul_f32_e32 v182, v79, v211
	v_add_f32_e32 v188, v188, v178
	v_fmac_f32_e32 v182, v78, v210
	ds_read_b128 v[208:211], v151
	v_add_f32_e32 v182, v183, v182
	v_add_f32_e32 v188, v188, v182
	s_waitcnt lgkmcnt(7)
	v_mul_f32_e32 v179, v77, v213
	v_fmac_f32_e32 v179, v76, v212
	v_mul_f32_e32 v178, v75, v215
	v_fmac_f32_e32 v178, v74, v214
	ds_read_b128 v[212:215], v152
	s_waitcnt lgkmcnt(7)
	v_mul_f32_e32 v183, v81, v217
	v_add_f32_e32 v178, v179, v178
	v_fmac_f32_e32 v183, v80, v216
	v_mul_f32_e32 v182, v73, v219
	v_add_f32_e32 v188, v188, v178
	v_fmac_f32_e32 v182, v72, v218
	ds_read_b128 v[216:219], v153
	v_add_f32_e32 v182, v183, v182
	v_add_f32_e32 v188, v188, v182
	s_waitcnt lgkmcnt(7)
	v_mul_f32_e32 v179, v69, v221
	v_fmac_f32_e32 v179, v68, v220
	v_mul_f32_e32 v178, v65, v223
	v_fmac_f32_e32 v178, v64, v222
	ds_read_b128 v[220:223], v154
	s_waitcnt lgkmcnt(7)
	v_mul_f32_e32 v183, v71, v225
	v_add_f32_e32 v178, v179, v178
	v_fmac_f32_e32 v183, v70, v224
	v_mul_f32_e32 v182, v67, v227
	v_add_f32_e32 v188, v188, v178
	v_fmac_f32_e32 v182, v66, v226
	ds_read_b128 v[224:227], v155
	v_add_f32_e32 v182, v183, v182
	v_add_f32_e32 v188, v188, v182
	s_waitcnt lgkmcnt(7)
	v_mul_f32_e32 v179, v93, v197
	v_fmac_f32_e32 v179, v92, v196
	v_mul_f32_e32 v178, v91, v199
	v_fmac_f32_e32 v178, v90, v198
	ds_read_b128 v[196:199], v156
	s_waitcnt lgkmcnt(7)
	v_mul_f32_e32 v183, v95, v201
	v_add_f32_e32 v178, v179, v178
	v_fmac_f32_e32 v183, v94, v200
	v_mul_f32_e32 v182, v89, v203
	v_add_f32_e32 v189, 0, v178
	v_fmac_f32_e32 v182, v88, v202
	ds_read_b128 v[200:203], v157
	v_add_f32_e32 v182, v183, v182
	v_add_f32_e32 v189, v189, v182
	s_waitcnt lgkmcnt(7)
	v_mul_f32_e32 v179, v85, v205
	v_fmac_f32_e32 v179, v84, v204
	v_mul_f32_e32 v178, v83, v207
	v_fmac_f32_e32 v178, v82, v206
	ds_read_b128 v[204:207], v158
	s_waitcnt lgkmcnt(7)
	v_mul_f32_e32 v183, v87, v209
	v_add_f32_e32 v178, v179, v178
	v_fmac_f32_e32 v183, v86, v208
	v_mul_f32_e32 v182, v79, v211
	v_add_f32_e32 v189, v189, v178
	v_fmac_f32_e32 v182, v78, v210
	ds_read_b128 v[208:211], v159
	v_add_f32_e32 v182, v183, v182
	v_add_f32_e32 v189, v189, v182
	s_waitcnt lgkmcnt(7)
	v_mul_f32_e32 v179, v77, v213
	v_fmac_f32_e32 v179, v76, v212
	v_mul_f32_e32 v178, v75, v215
	v_fmac_f32_e32 v178, v74, v214
	ds_read_b128 v[212:215], v160
	s_waitcnt lgkmcnt(7)
	v_mul_f32_e32 v183, v81, v217
	v_add_f32_e32 v178, v179, v178
	v_fmac_f32_e32 v183, v80, v216
	v_mul_f32_e32 v182, v73, v219
	v_add_f32_e32 v189, v189, v178
	v_fmac_f32_e32 v182, v72, v218
	ds_read_b128 v[216:219], v161
	v_add_f32_e32 v182, v183, v182
	v_add_f32_e32 v189, v189, v182
	s_waitcnt lgkmcnt(7)
	v_mul_f32_e32 v179, v69, v221
	v_fmac_f32_e32 v179, v68, v220
	v_mul_f32_e32 v178, v65, v223
	v_fmac_f32_e32 v178, v64, v222
	ds_read_b128 v[220:223], v162
	s_waitcnt lgkmcnt(7)
	v_mul_f32_e32 v183, v71, v225
	v_add_f32_e32 v178, v179, v178
	v_fmac_f32_e32 v183, v70, v224
	v_mul_f32_e32 v182, v67, v227
	v_add_f32_e32 v189, v189, v178
	v_fmac_f32_e32 v182, v66, v226
	ds_read_b128 v[224:227], v163
	v_add_f32_e32 v182, v183, v182
	v_add_f32_e32 v189, v189, v182
	s_waitcnt lgkmcnt(7)
	v_mul_f32_e32 v93, v93, v197
	v_mul_f32_e32 v91, v91, v199
	v_fmac_f32_e32 v93, v92, v196
	v_fmac_f32_e32 v91, v90, v198
	v_add_f32_e32 v90, v93, v91
	s_waitcnt lgkmcnt(6)
; #define LAS __attribute__((address_space(3)))
; DI float sigmoidf_(float x) { return __builtin_amdgcn_rcpf(1.0f + __expf(-x)); }
; DI float softplusf_(float x) { return fmaxf(x, 0.f) + log1pf(__expf(-fabsf(x))); }
; template <int MODE, bool SB  > DI void norm_phase(const Params& P, const Frame& F, int L, const void* src_, const float* gain, bool combine) {
;     ...
;                 for (int j = 0; j < 8; ++j) { const f32x4 w = *(const LAS f32x4*)(F.lds + (size_t)(q * D + 256 * j + 4 * F.lane) * 4); t += (v[j][0] * w[0] + v[j][1] * w[1]) + (v[j][2] * w[2] + v[j][3] * w[3]); }
;                 s[q] = t; if ((q & 3) == 3) asm volatile("" ::: "memory"); }
; #pragma unroll
;             for (int i = 0; i < 8; ++i) { const bool hi = (F.lane & 32) != 0; const float send = hi ? s[i] : s[i + 8], keep = hi ? s[i + 8] : s[i]; s[i] = keep + shx<32>(send); }
; #pragma unroll
;             for (int i = 0; i < 4; ++i) { const bool hi = (F.lane & 16) != 0; const float send = hi ? s[i] : s[i + 4], keep = hi ? s[i + 4] : s[i]; s[i] = keep + shx<16>(send); }
; #pragma unroll
;             for (int i = 0; i < 2; ++i) { const bool hi = (F.lane & 8) != 0; const float send = hi ? s[i] : s[i + 2], keep = hi ? s[i + 2] : s[i]; s[i] = keep + shx<8>(send); }
;             { const bool hi = (F.lane & 4) != 0; const float send = hi ? s[0] : s[1], keep = hi ? s[1] : s[0]; s[0] = keep + shx<4>(send); }
;             float mine = s[0]; mine += shx<2>(mine); mine += shx<1>(mine);
;             if ((F.lane & 3) == 0) { const int gi = ((F.lane >> 5) & 1) * 8 + ((F.lane >> 4) & 1) * 4 + ((F.lane >> 3) & 1) * 2 + ((F.lane >> 2) & 1), h = gi & 3; float r;
;                 if (gi < 4) r = sigmoidf_(mine);
;                 else if (gi < 8) r = -__expf(P.in[I_DN_A_LOG][L * 4 + h]) * softplusf_(mine + P.in[I_DN_DT_BIAS][L * 4 + h]);
;                 else if (gi < 12) r = mine + P.in[I_ML_I_BIAS][L * 4 + h];
;                 else r = -softplusf_(-(mine + P.in[I_ML_F_BIAS][L * 4 + h]));
;                 ((float*)(ws + WS_GD))[(size_t)row * 16 + gi] = r; }
	v_mul_f32_e32 v95, v95, v201
	v_mul_f32_e32 v89, v89, v203
	v_add_f32_e32 v178, 0, v90
	v_fmac_f32_e32 v95, v94, v200
	v_fmac_f32_e32 v89, v88, v202
	v_add_f32_e32 v88, v95, v89
	v_add_f32_e32 v88, v178, v88
	s_waitcnt lgkmcnt(5)
	v_mul_f32_e32 v85, v85, v205
	v_mul_f32_e32 v83, v83, v207
	v_fmac_f32_e32 v85, v84, v204
	v_fmac_f32_e32 v83, v82, v206
	v_add_f32_e32 v82, v85, v83
	s_waitcnt lgkmcnt(4)
	v_mul_f32_e32 v87, v87, v209
	v_mul_f32_e32 v79, v79, v211
	v_add_f32_e32 v88, v88, v82
	v_fmac_f32_e32 v87, v86, v208
	v_fmac_f32_e32 v79, v78, v210
	v_add_f32_e32 v78, v87, v79
	v_add_f32_e32 v78, v88, v78
	s_waitcnt lgkmcnt(3)
	v_mul_f32_e32 v77, v77, v213
	v_mul_f32_e32 v75, v75, v215
	v_fmac_f32_e32 v77, v76, v212
	v_fmac_f32_e32 v75, v74, v214
	v_add_f32_e32 v74, v77, v75
	s_waitcnt lgkmcnt(2)
	v_mul_f32_e32 v79, v81, v217
	v_mul_f32_e32 v73, v73, v219
	v_add_f32_e32 v78, v78, v74
	v_fmac_f32_e32 v79, v80, v216
	v_fmac_f32_e32 v73, v72, v218
	v_add_f32_e32 v72, v79, v73
	v_add_f32_e32 v72, v78, v72
	s_waitcnt lgkmcnt(1)
	v_mul_f32_e32 v69, v69, v221
	v_mul_f32_e32 v65, v65, v223
	v_fmac_f32_e32 v69, v68, v220
	v_fmac_f32_e32 v65, v64, v222
	v_add_f32_e32 v64, v69, v65
	s_waitcnt lgkmcnt(0)
	v_mul_f32_e32 v65, v71, v225
	v_mul_f32_e32 v67, v67, v227
	v_fmac_f32_e32 v65, v70, v224
	v_fmac_f32_e32 v67, v66, v226
	v_add_f32_e32 v64, v72, v64
	v_add_f32_e32 v65, v65, v67
	v_add_f32_e32 v64, v64, v65
	v_cndmask_b32_e64 v65, v47, v175, s[4:5]
	ds_bpermute_b32 v65, v98, v65
	v_cndmask_b32_e64 v66, v96, v176, s[4:5]
	ds_bpermute_b32 v66, v98, v66
	v_cndmask_b32_e64 v67, v97, v177, s[4:5]
	ds_bpermute_b32 v67, v98, v67
	v_cndmask_b32_e64 v47, v175, v47, s[4:5]
	s_waitcnt lgkmcnt(2)
	v_add_f32_e32 v47, v47, v65
	v_cndmask_b32_e64 v65, v176, v96, s[4:5]
	s_waitcnt lgkmcnt(1)
	v_add_f32_e32 v65, v65, v66
	v_cndmask_b32_e64 v66, v177, v97, s[4:5]
	s_waitcnt lgkmcnt(0)
	v_add_f32_e32 v66, v66, v67
	v_cndmask_b32_e64 v67, v170, v186, s[4:5]
	ds_bpermute_b32 v67, v98, v67
	v_cndmask_b32_e64 v69, v171, v187, s[4:5]
	ds_bpermute_b32 v69, v98, v69
	v_cndmask_b32_e64 v70, v172, v188, s[4:5]
	ds_bpermute_b32 v70, v98, v70
	v_cndmask_b32_e64 v68, v186, v170, s[4:5]
	s_waitcnt lgkmcnt(2)
	v_add_f32_e32 v67, v68, v67
	v_cndmask_b32_e64 v68, v187, v171, s[4:5]
	s_waitcnt lgkmcnt(1)
	v_add_f32_e32 v68, v68, v69
	v_cndmask_b32_e64 v69, v188, v172, s[4:5]
	s_waitcnt lgkmcnt(0)
	v_add_f32_e32 v69, v69, v70
	v_cndmask_b32_e64 v70, v173, v189, s[4:5]
	v_cndmask_b32_e64 v72, v174, v64, s[4:5]
	ds_bpermute_b32 v70, v98, v70
	ds_bpermute_b32 v72, v98, v72
	v_cndmask_b32_e64 v71, v189, v173, s[4:5]
	v_cndmask_b32_e64 v64, v64, v174, s[4:5]
	v_cndmask_b32_e64 v73, v47, v68, s[8:9]
	s_waitcnt lgkmcnt(1)
	v_add_f32_e32 v70, v71, v70
	s_waitcnt lgkmcnt(0)
	v_add_f32_e32 v64, v64, v72
	v_cndmask_b32_e64 v47, v68, v47, s[8:9]
	v_cndmask_b32_e64 v68, v65, v69, s[8:9]
	v_cndmask_b32_e64 v65, v69, v65, s[8:9]
	v_cndmask_b32_e64 v69, v66, v70, s[8:9]
	v_cndmask_b32_e64 v71, v67, v64, s[8:9]
	ds_swizzle_b32 v73, v73 offset:swizzle(SWAP,16)
	ds_swizzle_b32 v68, v68 offset:swizzle(SWAP,16)
	ds_swizzle_b32 v69, v69 offset:swizzle(SWAP,16)
	ds_swizzle_b32 v71, v71 offset:swizzle(SWAP,16)
	v_cndmask_b32_e64 v66, v70, v66, s[8:9]
	v_cndmask_b32_e64 v64, v64, v67, s[8:9]
	s_waitcnt lgkmcnt(3)
	v_add_f32_e32 v47, v47, v73
	s_waitcnt lgkmcnt(2)
	v_add_f32_e32 v65, v65, v68
	s_waitcnt lgkmcnt(1)
	v_add_f32_e32 v66, v66, v69
	s_waitcnt lgkmcnt(0)
	v_add_f32_e32 v64, v64, v71
	v_cndmask_b32_e64 v67, v47, v66, s[10:11]
	v_cndmask_b32_e64 v68, v65, v64, s[10:11]
	ds_swizzle_b32 v67, v67 offset:swizzle(SWAP,8)
	ds_swizzle_b32 v68, v68 offset:swizzle(SWAP,8)
	v_cndmask_b32_e64 v47, v66, v47, s[10:11]
	v_cndmask_b32_e64 v64, v64, v65, s[10:11]
	s_waitcnt lgkmcnt(1)
	v_add_f32_e32 v47, v47, v67
	s_waitcnt lgkmcnt(0)
	v_add_f32_e32 v64, v64, v68
	v_cndmask_b32_e64 v65, v47, v64, s[12:13]
	ds_swizzle_b32 v65, v65 offset:swizzle(SWAP,4)
	v_cndmask_b32_e64 v47, v64, v47, s[12:13]
	s_waitcnt lgkmcnt(0)
	v_add_f32_e32 v47, v47, v65
	s_nop 1
	v_add_f32_dpp v47, v47, v47 quad_perm:[2,3,0,1] row_mask:0xf bank_mask:0xf bound_ctrl:1
	s_nop 1
	v_mov_b32_dpp v64, v47 quad_perm:[1,0,3,2] row_mask:0xf bank_mask:0xf bound_ctrl:1
	s_and_saveexec_b64 s[20:21], s[14:15]
	s_cbranch_execz .LBB0_1647
	v_add_f32_e32 v47, v47, v64
	s_and_saveexec_b64 s[24:25], s[16:17]
	s_xor_b64 s[24:25], exec, s[24:25]
	s_cbranch_execz .LBB0_1659
	s_and_saveexec_b64 s[26:27], s[6:7]
	s_xor_b64 s[26:27], exec, s[26:27]
	s_cbranch_execz .LBB0_1656
	s_and_saveexec_b64 s[28:29], s[18:19]
	s_xor_b64 s[28:29], exec, s[28:29]
	s_cbranch_execz .LBB0_1653
	v_mov_b32_e32 v64, v190
	v_add_f32_e32 v64, v47, v64
